# MoE (w1|w3) absmax pass reads 1 KB contiguous per wave-load (lane = 4 columns, dwordx4; item = 256 cols x 64 rows)
# speedup vs baseline: 1.0012x; 1.0012x over previous
; __device__ __forceinline__ void w13_absmax_item(const float* W1, const float* W3, const float* gain, unsigned* amax, int item, int lane, bool dry = false) {
;     const int kq = item & 3, cb = (item >> 2) % (DFF / 64), mat = (item >> 2) / (DFF / 64); const float* W = mat ? W3 : W1; const int j = cb * 64 + lane;
;     float am = 0.f;
; #pragma unroll 1
;     for (int kb = 0; kb < 8; ++kb) { float tv[32];
; #pragma unroll
;         for (int i = 0; i < 32; ++i) tv[i] = W[(size_t)(kq * 256 + kb * 32 + i) * DFF + j];
; #pragma unroll
;         for (int i = 0; i < 32; ++i) am = fmaxf(am, fabsf(tv[i] * gain[kq * 256 + kb * 32 + i])); }
; __device__ __forceinline__ void phase_moe_weights_a(const Frame& F, const Params& P, int mi, bool dry) {
;     const int gw = F.bid * NWAVES + F.wave, NGW = F.G * NWAVES, lane = F.lane; constexpr int I_A = 2 * (DFF / 64) * 4;
;     for (int it = gw; it < NE * (I_A + I_W2A); it += NGW) { const int e = it / (I_A + I_W2A), r = it - e * (I_A + I_W2A); const size_t eo = ((size_t)mi * NE + e) * D * DFF;
;         if (r < I_A) w13_absmax_item(P.in[28] + eo, P.in[29] + eo, P.in[23] + 1 * D, (unsigned*)(F.ws + CTL_AMAX) + (1 + e) * 2 * DFF, r, lane, dry);
;         else w2_absmax_item(P.in[30] + eo, (unsigned*)(F.ws + CTL_AMAX) + AMAX_W2 + 1 + e, r - I_A, lane, dry); }
.LBB0_1397:
	s_cmpk_ge_i32 s25, 0xe0
	s_cselect_b32 s12, 1, 0
	s_mul_i32 s8, s12, 0xe0
	s_sub_i32 s8, s25, s8
	s_mul_i32 s9, s8, 0x124a
	s_lshr_b32 s9, s9, 16
	s_mul_i32 s10, s9, 14
	s_sub_i32 s13, s8, s10
	v_readlane_b32 s10, v254, 0
	v_readlane_b32 s11, v254, 1
	v_readlane_b32 s14, v254, 2
	v_readlane_b32 s15, v254, 3
	v_lshlrev_b32_e32 v10, 4, v85
	v_mov_b32_e32 v11, 0
	s_cmp_eq_u32 s12, 0
	s_cselect_b32 s10, s10, s14
	s_cselect_b32 s11, s11, s15
	s_add_u32 s10, s10, s20
	s_addc_u32 s11, s11, s19
	s_mul_i32 s14, s6, 0xe00000
	s_mul_hi_u32 s15, s6, 0xe00000
	s_add_u32 s10, s10, s14
	s_addc_u32 s11, s11, s15
	s_mul_i32 s14, s9, 0xe0000
	s_add_u32 s10, s10, s14
	s_addc_u32 s11, s11, 0
	s_lshl_b32 s14, s13, 10
	s_add_u32 s10, s10, s14
	s_addc_u32 s11, s11, 0
	v_lshl_add_u64 v[4:5], s[10:11], 0, v[10:11]
	v_readlane_b32 s10, v253, 51
	v_readlane_b32 s11, v253, 52
	v_mov_b32_e32 v6, 0
	v_mov_b32_e32 v7, 0
	v_mov_b32_e32 v8, 0
	v_mov_b32_e32 v9, 0
	s_lshl_b32 s14, s9, 8
	s_add_u32 s10, s10, s14
	s_addc_u32 s11, s11, 0
	s_mov_b64 s[26:27], 0x3800
	s_mov_b32 s8, 0
.Lpaw_loop:
	global_load_dwordx4 v[116:119], v[4:5], off
	v_lshl_add_u64 v[4:5], v[4:5], 0, s[26:27]
	global_load_dwordx4 v[120:123], v[4:5], off
	v_lshl_add_u64 v[4:5], v[4:5], 0, s[26:27]
	global_load_dwordx4 v[124:127], v[4:5], off
	v_lshl_add_u64 v[4:5], v[4:5], 0, s[26:27]
	global_load_dwordx4 v[128:131], v[4:5], off
	v_lshl_add_u64 v[4:5], v[4:5], 0, s[26:27]
	global_load_dwordx4 v[132:135], v[4:5], off
	v_lshl_add_u64 v[4:5], v[4:5], 0, s[26:27]
	global_load_dwordx4 v[136:139], v[4:5], off
	v_lshl_add_u64 v[4:5], v[4:5], 0, s[26:27]
	global_load_dwordx4 v[140:143], v[4:5], off
	v_lshl_add_u64 v[4:5], v[4:5], 0, s[26:27]
	global_load_dwordx4 v[144:147], v[4:5], off
	v_lshl_add_u64 v[4:5], v[4:5], 0, s[26:27]
	global_load_dwordx4 v[148:151], v[4:5], off
	v_lshl_add_u64 v[4:5], v[4:5], 0, s[26:27]
	global_load_dwordx4 v[152:155], v[4:5], off
	v_lshl_add_u64 v[4:5], v[4:5], 0, s[26:27]
	global_load_dwordx4 v[156:159], v[4:5], off
	v_lshl_add_u64 v[4:5], v[4:5], 0, s[26:27]
	global_load_dwordx4 v[160:163], v[4:5], off
	v_lshl_add_u64 v[4:5], v[4:5], 0, s[26:27]
	global_load_dwordx4 v[166:169], v[4:5], off
	v_lshl_add_u64 v[4:5], v[4:5], 0, s[26:27]
	global_load_dwordx4 v[170:173], v[4:5], off
	v_lshl_add_u64 v[4:5], v[4:5], 0, s[26:27]
	global_load_dwordx4 v[174:177], v[4:5], off
	v_lshl_add_u64 v[4:5], v[4:5], 0, s[26:27]
	global_load_dwordx4 v[178:181], v[4:5], off
	v_lshl_add_u64 v[4:5], v[4:5], 0, s[26:27]
	global_load_dwordx4 v[182:185], v[4:5], off
	v_lshl_add_u64 v[4:5], v[4:5], 0, s[26:27]
	global_load_dwordx4 v[186:189], v[4:5], off
	v_lshl_add_u64 v[4:5], v[4:5], 0, s[26:27]
	global_load_dwordx4 v[190:193], v[4:5], off
	v_lshl_add_u64 v[4:5], v[4:5], 0, s[26:27]
	global_load_dwordx4 v[194:197], v[4:5], off
	v_lshl_add_u64 v[4:5], v[4:5], 0, s[26:27]
	global_load_dwordx4 v[198:201], v[4:5], off
	v_lshl_add_u64 v[4:5], v[4:5], 0, s[26:27]
	global_load_dwordx4 v[202:205], v[4:5], off
	v_lshl_add_u64 v[4:5], v[4:5], 0, s[26:27]
	global_load_dwordx4 v[206:209], v[4:5], off
	v_lshl_add_u64 v[4:5], v[4:5], 0, s[26:27]
	global_load_dwordx4 v[210:213], v[4:5], off
	v_lshl_add_u64 v[4:5], v[4:5], 0, s[26:27]
	global_load_dwordx4 v[214:217], v[4:5], off
	v_lshl_add_u64 v[4:5], v[4:5], 0, s[26:27]
	global_load_dwordx4 v[218:221], v[4:5], off
	v_lshl_add_u64 v[4:5], v[4:5], 0, s[26:27]
	global_load_dwordx4 v[222:225], v[4:5], off
	v_lshl_add_u64 v[4:5], v[4:5], 0, s[26:27]
	global_load_dwordx4 v[226:229], v[4:5], off
	v_lshl_add_u64 v[4:5], v[4:5], 0, s[26:27]
	global_load_dwordx4 v[230:233], v[4:5], off
	v_lshl_add_u64 v[4:5], v[4:5], 0, s[26:27]
	global_load_dwordx4 v[234:237], v[4:5], off
	v_lshl_add_u64 v[4:5], v[4:5], 0, s[26:27]
	global_load_dwordx4 v[238:241], v[4:5], off
	v_lshl_add_u64 v[4:5], v[4:5], 0, s[26:27]
	global_load_dwordx4 v[242:245], v[4:5], off
	v_lshl_add_u64 v[4:5], v[4:5], 0, s[26:27]
	global_load_dwordx4 v[56:59], v250, s[10:11] offset:0
	global_load_dwordx4 v[60:63], v250, s[10:11] offset:16
	global_load_dwordx4 v[64:67], v250, s[10:11] offset:32
	global_load_dwordx4 v[68:71], v250, s[10:11] offset:48
	global_load_dwordx4 v[72:75], v250, s[10:11] offset:64
	global_load_dwordx4 v[76:79], v250, s[10:11] offset:80
	global_load_dwordx4 v[80:83], v250, s[10:11] offset:96
	global_load_dwordx4 v[88:91], v250, s[10:11] offset:112
	s_add_u32 s10, s10, 0x80
	s_addc_u32 s11, s11, 0
	s_add_i32 s8, s8, 1
	s_cmp_lg_u32 s8, 2
	s_waitcnt vmcnt(0)
; __device__ __forceinline__ void w13_absmax_item(const float* W1, const float* W3, const float* gain, unsigned* amax, int item, int lane, bool dry = false) {
;     ...
;     for (int kb = 0; kb < 8; ++kb) { float tv[32];
; #pragma unroll
;         for (int i = 0; i < 32; ++i) tv[i] = W[(size_t)(kq * 256 + kb * 32 + i) * DFF + j];
; #pragma unroll
;         for (int i = 0; i < 32; ++i) am = fmaxf(am, fabsf(tv[i] * gain[kq * 256 + kb * 32 + i])); }
	v_pk_mul_f32 v[116:117], v[116:117], v[56:57] op_sel_hi:[1,0]
	v_pk_mul_f32 v[118:119], v[118:119], v[56:57] op_sel_hi:[1,0]
	v_pk_mul_f32 v[120:121], v[120:121], v[56:57] op_sel:[0,1] op_sel_hi:[1,1]
	v_pk_mul_f32 v[122:123], v[122:123], v[56:57] op_sel:[0,1] op_sel_hi:[1,1]
	v_pk_mul_f32 v[124:125], v[124:125], v[58:59] op_sel_hi:[1,0]
	v_pk_mul_f32 v[126:127], v[126:127], v[58:59] op_sel_hi:[1,0]
	v_pk_mul_f32 v[128:129], v[128:129], v[58:59] op_sel:[0,1] op_sel_hi:[1,1]
	v_pk_mul_f32 v[130:131], v[130:131], v[58:59] op_sel:[0,1] op_sel_hi:[1,1]
	v_pk_mul_f32 v[132:133], v[132:133], v[60:61] op_sel_hi:[1,0]
	v_pk_mul_f32 v[134:135], v[134:135], v[60:61] op_sel_hi:[1,0]
	v_pk_mul_f32 v[136:137], v[136:137], v[60:61] op_sel:[0,1] op_sel_hi:[1,1]
	v_pk_mul_f32 v[138:139], v[138:139], v[60:61] op_sel:[0,1] op_sel_hi:[1,1]
	v_pk_mul_f32 v[140:141], v[140:141], v[62:63] op_sel_hi:[1,0]
	v_pk_mul_f32 v[142:143], v[142:143], v[62:63] op_sel_hi:[1,0]
	v_pk_mul_f32 v[144:145], v[144:145], v[62:63] op_sel:[0,1] op_sel_hi:[1,1]
	v_pk_mul_f32 v[146:147], v[146:147], v[62:63] op_sel:[0,1] op_sel_hi:[1,1]
	v_pk_mul_f32 v[148:149], v[148:149], v[64:65] op_sel_hi:[1,0]
	v_pk_mul_f32 v[150:151], v[150:151], v[64:65] op_sel_hi:[1,0]
	v_pk_mul_f32 v[152:153], v[152:153], v[64:65] op_sel:[0,1] op_sel_hi:[1,1]
	v_pk_mul_f32 v[154:155], v[154:155], v[64:65] op_sel:[0,1] op_sel_hi:[1,1]
	v_pk_mul_f32 v[156:157], v[156:157], v[66:67] op_sel_hi:[1,0]
	v_pk_mul_f32 v[158:159], v[158:159], v[66:67] op_sel_hi:[1,0]
	v_pk_mul_f32 v[160:161], v[160:161], v[66:67] op_sel:[0,1] op_sel_hi:[1,1]
	v_pk_mul_f32 v[162:163], v[162:163], v[66:67] op_sel:[0,1] op_sel_hi:[1,1]
	v_pk_mul_f32 v[166:167], v[166:167], v[68:69] op_sel_hi:[1,0]
	v_pk_mul_f32 v[168:169], v[168:169], v[68:69] op_sel_hi:[1,0]
	v_pk_mul_f32 v[170:171], v[170:171], v[68:69] op_sel:[0,1] op_sel_hi:[1,1]
	v_pk_mul_f32 v[172:173], v[172:173], v[68:69] op_sel:[0,1] op_sel_hi:[1,1]
	v_pk_mul_f32 v[174:175], v[174:175], v[70:71] op_sel_hi:[1,0]
	v_pk_mul_f32 v[176:177], v[176:177], v[70:71] op_sel_hi:[1,0]
	v_pk_mul_f32 v[178:179], v[178:179], v[70:71] op_sel:[0,1] op_sel_hi:[1,1]
	v_pk_mul_f32 v[180:181], v[180:181], v[70:71] op_sel:[0,1] op_sel_hi:[1,1]
	v_pk_mul_f32 v[182:183], v[182:183], v[72:73] op_sel_hi:[1,0]
	v_pk_mul_f32 v[184:185], v[184:185], v[72:73] op_sel_hi:[1,0]
	v_pk_mul_f32 v[186:187], v[186:187], v[72:73] op_sel:[0,1] op_sel_hi:[1,1]
	v_pk_mul_f32 v[188:189], v[188:189], v[72:73] op_sel:[0,1] op_sel_hi:[1,1]
	v_pk_mul_f32 v[190:191], v[190:191], v[74:75] op_sel_hi:[1,0]
	v_pk_mul_f32 v[192:193], v[192:193], v[74:75] op_sel_hi:[1,0]
	v_pk_mul_f32 v[194:195], v[194:195], v[74:75] op_sel:[0,1] op_sel_hi:[1,1]
	v_pk_mul_f32 v[196:197], v[196:197], v[74:75] op_sel:[0,1] op_sel_hi:[1,1]
	v_pk_mul_f32 v[198:199], v[198:199], v[76:77] op_sel_hi:[1,0]
	v_pk_mul_f32 v[200:201], v[200:201], v[76:77] op_sel_hi:[1,0]
	v_pk_mul_f32 v[202:203], v[202:203], v[76:77] op_sel:[0,1] op_sel_hi:[1,1]
	v_pk_mul_f32 v[204:205], v[204:205], v[76:77] op_sel:[0,1] op_sel_hi:[1,1]
	v_pk_mul_f32 v[206:207], v[206:207], v[78:79] op_sel_hi:[1,0]
	v_pk_mul_f32 v[208:209], v[208:209], v[78:79] op_sel_hi:[1,0]
	v_pk_mul_f32 v[210:211], v[210:211], v[78:79] op_sel:[0,1] op_sel_hi:[1,1]
	v_pk_mul_f32 v[212:213], v[212:213], v[78:79] op_sel:[0,1] op_sel_hi:[1,1]
	v_pk_mul_f32 v[214:215], v[214:215], v[80:81] op_sel_hi:[1,0]
	v_pk_mul_f32 v[216:217], v[216:217], v[80:81] op_sel_hi:[1,0]
	v_pk_mul_f32 v[218:219], v[218:219], v[80:81] op_sel:[0,1] op_sel_hi:[1,1]
	v_pk_mul_f32 v[220:221], v[220:221], v[80:81] op_sel:[0,1] op_sel_hi:[1,1]
	v_pk_mul_f32 v[222:223], v[222:223], v[82:83] op_sel_hi:[1,0]
	v_pk_mul_f32 v[224:225], v[224:225], v[82:83] op_sel_hi:[1,0]
	v_pk_mul_f32 v[226:227], v[226:227], v[82:83] op_sel:[0,1] op_sel_hi:[1,1]
	v_pk_mul_f32 v[228:229], v[228:229], v[82:83] op_sel:[0,1] op_sel_hi:[1,1]
	v_pk_mul_f32 v[230:231], v[230:231], v[88:89] op_sel_hi:[1,0]
	v_pk_mul_f32 v[232:233], v[232:233], v[88:89] op_sel_hi:[1,0]
	v_pk_mul_f32 v[234:235], v[234:235], v[88:89] op_sel:[0,1] op_sel_hi:[1,1]
	v_pk_mul_f32 v[236:237], v[236:237], v[88:89] op_sel:[0,1] op_sel_hi:[1,1]
	v_pk_mul_f32 v[238:239], v[238:239], v[90:91] op_sel_hi:[1,0]
	v_pk_mul_f32 v[240:241], v[240:241], v[90:91] op_sel_hi:[1,0]
	v_pk_mul_f32 v[242:243], v[242:243], v[90:91] op_sel:[0,1] op_sel_hi:[1,1]
	v_pk_mul_f32 v[244:245], v[244:245], v[90:91] op_sel:[0,1] op_sel_hi:[1,1]
	v_max3_f32 v6, v6, |v116|, |v120|
	v_max3_f32 v7, v7, |v117|, |v121|
	v_max3_f32 v8, v8, |v118|, |v122|
	v_max3_f32 v9, v9, |v119|, |v123|
	v_max3_f32 v6, v6, |v124|, |v128|
	v_max3_f32 v7, v7, |v125|, |v129|
	v_max3_f32 v8, v8, |v126|, |v130|
	v_max3_f32 v9, v9, |v127|, |v131|
	v_max3_f32 v6, v6, |v132|, |v136|
	v_max3_f32 v7, v7, |v133|, |v137|
	v_max3_f32 v8, v8, |v134|, |v138|
	v_max3_f32 v9, v9, |v135|, |v139|
	v_max3_f32 v6, v6, |v140|, |v144|
	v_max3_f32 v7, v7, |v141|, |v145|
	v_max3_f32 v8, v8, |v142|, |v146|
	v_max3_f32 v9, v9, |v143|, |v147|
	v_max3_f32 v6, v6, |v148|, |v152|
	v_max3_f32 v7, v7, |v149|, |v153|
	v_max3_f32 v8, v8, |v150|, |v154|
	v_max3_f32 v9, v9, |v151|, |v155|
	v_max3_f32 v6, v6, |v156|, |v160|
	v_max3_f32 v7, v7, |v157|, |v161|
	v_max3_f32 v8, v8, |v158|, |v162|
	v_max3_f32 v9, v9, |v159|, |v163|
	v_max3_f32 v6, v6, |v166|, |v170|
	v_max3_f32 v7, v7, |v167|, |v171|
	v_max3_f32 v8, v8, |v168|, |v172|
	v_max3_f32 v9, v9, |v169|, |v173|
	v_max3_f32 v6, v6, |v174|, |v178|
	v_max3_f32 v7, v7, |v175|, |v179|
	v_max3_f32 v8, v8, |v176|, |v180|
	v_max3_f32 v9, v9, |v177|, |v181|
	v_max3_f32 v6, v6, |v182|, |v186|
	v_max3_f32 v7, v7, |v183|, |v187|
	v_max3_f32 v8, v8, |v184|, |v188|
	v_max3_f32 v9, v9, |v185|, |v189|
	v_max3_f32 v6, v6, |v190|, |v194|
	v_max3_f32 v7, v7, |v191|, |v195|
	v_max3_f32 v8, v8, |v192|, |v196|
	v_max3_f32 v9, v9, |v193|, |v197|
	v_max3_f32 v6, v6, |v198|, |v202|
	v_max3_f32 v7, v7, |v199|, |v203|
	v_max3_f32 v8, v8, |v200|, |v204|
	v_max3_f32 v9, v9, |v201|, |v205|
	v_max3_f32 v6, v6, |v206|, |v210|
	v_max3_f32 v7, v7, |v207|, |v211|
	v_max3_f32 v8, v8, |v208|, |v212|
	v_max3_f32 v9, v9, |v209|, |v213|
	v_max3_f32 v6, v6, |v214|, |v218|
	v_max3_f32 v7, v7, |v215|, |v219|
	v_max3_f32 v8, v8, |v216|, |v220|
	v_max3_f32 v9, v9, |v217|, |v221|
	v_max3_f32 v6, v6, |v222|, |v226|
	v_max3_f32 v7, v7, |v223|, |v227|
	v_max3_f32 v8, v8, |v224|, |v228|
	v_max3_f32 v9, v9, |v225|, |v229|
	v_max3_f32 v6, v6, |v230|, |v234|
	v_max3_f32 v7, v7, |v231|, |v235|
	v_max3_f32 v8, v8, |v232|, |v236|
	v_max3_f32 v9, v9, |v233|, |v237|
	v_max3_f32 v6, v6, |v238|, |v242|
	v_max3_f32 v7, v7, |v239|, |v243|
	v_max3_f32 v8, v8, |v240|, |v244|
	v_max3_f32 v9, v9, |v241|, |v245|
	s_cbranch_scc1 .Lpaw_loop
; __device__ __forceinline__ void w13_absmax_item(const float* W1, const float* W3, const float* gain, unsigned* amax, int item, int lane, bool dry = false) {
;     ...
;     if (!dry) atomicMax(amax + 256 * (j >> 7) + (j & 127) + 128 * mat, __float_as_uint(am));
	s_add_i32 s14, s6, 1
	s_mul_i32 s14, s14, 0x1c00
	s_lshl_b32 s15, s13, 9
	s_add_i32 s14, s14, s15
	s_lshl_b32 s15, s12, 7
	s_add_i32 s14, s14, s15
	s_lshl_b32 s14, s14, 2
	s_add_u32 s10, s17, s14
	s_addc_u32 s11, s18, 0
	v_lshrrev_b32_e32 v10, 5, v85
	v_and_b32_e32 v12, 31, v85
	v_lshlrev_b32_e32 v10, 10, v10
	v_lshl_add_u32 v10, v12, 4, v10
	v_mov_b32_e32 v11, 0
	v_lshl_add_u64 v[2:3], s[10:11], 0, v[10:11]
	flat_atomic_umax v[2:3], v6
	flat_atomic_umax v[2:3], v7 offset:4
	flat_atomic_umax v[2:3], v8 offset:8
	flat_atomic_umax v[2:3], v9 offset:12
	s_mov_b64 s[6:7], exec
	s_branch .LBB0_1389
